# strategy: one static s_setprio 1 for the younger wave half (waves 4-7) across the rsub and attention phases, reset at phase exit
# baseline (speedup 1.0000x reference)
; DI void phase_attn(const Frame& F, int j) {
;     ...
;     LAS bf16_t* Ks = (LAS bf16_t*)(F.lds + A_KS); LAS bf16_t* Vt = (LAS bf16_t*)(F.lds + A_VT); LAS float* bT = (LAS float*)(F.lds + A_BIAS);
;     const int r = F.lane & 31, h = F.lane >> 5; int kvh_tab = -1;
;     for (int u = F.vcu; u < NB * 2 * 32; u += F.G) {
;         const int qb = u & 31, kvh = (u >> 5) & 1, b = u >> 6; const int q0 = qb * 128;
;         __syncthreads();
;         {
;             u32x4 kvr[6], vvr[6];
; #pragma unroll
;             for (int it = 0; it < 6; ++it) { const int cidx = F.tid + it * NTHR, key = cidx >> 3, part = cidx & 7, kp = q0 - 128 + key; const bool ok = kp >= 0 && kp < SEQ;
;                 const bf16_t* row = QKV + (size_t)(b * SEQ + (ok ? kp : q0)) * QKV_N + 1024 + kvh * 64 + part * 8; kvr[it] = *(const u32x4*)row; vvr[it] = *(const u32x4*)(row + 128);
;                 if (!ok) { kvr[it] = (u32x4){0u, 0u, 0u, 0u}; vvr[it] = (u32x4){0u, 0u, 0u, 0u}; } }
; #pragma unroll
;             for (int it = 0; it < 6; ++it) { const int cidx = F.tid + it * NTHR, key = cidx >> 3, part = cidx & 7;
;                 *(LAS u32x4*)(Ks + key * KS_STRIDE + part * 8) = kvr[it];
;                 const unsigned vw[4] = {vvr[it].x, vvr[it].y, vvr[it].z, vvr[it].w};
; #pragma unroll
;                 for (int i = 0; i < 4; ++i) { Vt[(part * 8 + 2 * i) * VT_STRIDE + key] = (bf16_t)(vw[i] & 0xffffu); Vt[(part * 8 + 2 * i + 1) * VT_STRIDE + key] = (bf16_t)(vw[i] >> 16); } }
;         }
;         if (kvh != kvh_tab) for (int i = F.tid; i < 8 * 257; i += NTHR) { const int hh = i / 257, idx = i % 257; bT[hh * 260 + idx] = F.ap->in[29][t5_bucket(idx - 128) * 16 + kvh * 8 + hh] * 1.44269504f; }
;         kvh_tab = kvh;
;         __syncthreads();
;         const int hh = F.wave, head = kvh * 8 + hh; const float sink = F.ap->in[27][j * 16 + head] * 1.44269504f;
;         for (int sub = 0; sub < 4; ++sub) {
;             const int qrel = 32 * sub + r;
;             const size_t qrow = (size_t)(b * SEQ + q0 + qrel);
;             bf16x8 Qf[4];
; #pragma unroll
;             for (int s = 0; s < 4; ++s) Qf[s] = *(const bf16x8*)(QKV + qrow * QKV_N + head * 64 + 16 * s + 8 * h);
;             f32x16 O0, O1;
; #pragma unroll
;             for (int i = 0; i < 16; ++i) { O0[i] = 0.f; O1[i] = 0.f; }
;             float mrun = sink, lrun = h ? 0.f : 1.f;
;             for (int kt = sub; kt < sub + 9; ++kt) {
.LBB0_305:
	v_bfe_u32 v4, v0, 5, 1
	v_lshlrev_b32_e32 v86, 2, v4
	v_and_b32_e32 v85, 31, v0
	v_or_b32_e32 v2, 1, v86
	v_sub_u32_e32 v2, v2, v85
	v_cmp_gt_u32_e64 s[40:41], s33, v2
	v_add_u32_e32 v2, 0x400, v80
	s_load_dwordx2 s[4:5], s[92:93], 0x128
	v_ashrrev_i32_e32 v118, 3, v2
	v_add_u32_e32 v2, 0x600, v80
	v_and_b32_e32 v1, 63, v0
	v_or_b32_e32 v3, 2, v86
	v_or_b32_e32 v5, 3, v86
	v_lshlrev_b32_e32 v0, 3, v0
	v_add_u32_e32 v81, 0x200, v80
	v_ashrrev_i32_e32 v119, 3, v2
	v_add_u32_e32 v2, 0x800, v80
	v_sub_u32_e32 v3, v3, v85
	v_sub_u32_e32 v5, v5, v85
	v_and_b32_e32 v0, 56, v0
	v_ashrrev_i32_e32 v116, 3, v80
	v_ashrrev_i32_e32 v117, 3, v81
	v_ashrrev_i32_e32 v120, 3, v2
	v_add_u32_e32 v2, 0xa00, v80
	s_ashr_i32 s22, s2, 6
	s_cmp_lt_u32 s22, 4
	s_cbranch_scc1 .Lattn_prio_done
	s_setprio 1
.Lattn_prio_done:
	s_movk_i32 s2, 0x310
	v_cmp_gt_u32_e64 s[42:43], s33, v3
	v_cmp_gt_u32_e64 s[44:45], s33, v5
	v_ashrrev_i32_e32 v121, 3, v2
	v_mul_lo_u32 v2, v116, s85
	v_lshlrev_b32_e32 v3, 1, v0
	v_mul_lo_u32 v5, v117, s85
	v_mad_u32_u24 v113, v85, s2, 0
	v_add3_u32 v122, 0, v2, v3
	v_mad_u32_u24 v2, v0, s2, 0
	v_add3_u32 v124, 0, v5, v3
	v_mul_lo_u32 v5, v118, s85
	s_movk_i32 s2, 0x808
	s_waitcnt lgkmcnt(0)
	s_add_u32 s94, s4, 0x38000000
	v_readlane_b32 s6, v253, 54
	v_lshl_add_u32 v123, v116, 1, v2
	v_lshl_add_u32 v125, v117, 1, v2
	v_add3_u32 v126, 0, v5, v3
	v_lshl_add_u32 v127, v118, 1, v2
	v_mul_lo_u32 v5, v119, s85
	v_lshl_add_u32 v129, v119, 1, v2
	v_lshl_add_u32 v131, v120, 1, v2
	v_lshl_add_u32 v133, v121, 1, v2
	v_cmp_gt_i32_e32 vcc, s2, v80
	s_mul_i32 s2, s22, 0x410
	v_max_i32_e32 v2, 0x608, v80
	s_addc_u32 s95, s5, 0
	s_lshl_b32 s23, s6, 4
	v_add3_u32 v128, 0, v5, v3
	v_mul_lo_u32 v5, v120, s85
	s_add_i32 s6, s2, 0
	v_sub_u32_e32 v2, v2, v80
	v_sub_u32_e32 v115, v86, v85
	v_add3_u32 v130, 0, v5, v3
	v_mul_lo_u32 v5, v121, s85
	s_add_i32 s6, s6, 0x19c00
	v_add_u32_e32 v2, 0x1ff, v2
	v_readlane_b32 s7, v253, 55
	v_add3_u32 v132, 0, v5, v3
	v_lshl_add_u32 v134, v115, 2, s6
	v_lshrrev_b32_e32 v3, 9, v2
	s_movk_i32 s6, 0x1ff
	v_writelane_b32 v254, s24, 4
	v_add_u32_e32 v3, 1, v3
	v_cmp_lt_u32_e64 s[6:7], s6, v2
	v_writelane_b32 v254, s25, 5
	v_mov_b32_e32 v87, v193
	v_writelane_b32 v255, s6, 20
	s_waitcnt vmcnt(0)
	v_and_b32_e32 v135, 0xfffffe, v3
	v_writelane_b32 v254, s56, 0
	v_lshlrev_b32_e32 v192, 4, v4
	v_writelane_b32 v255, s7, 21
	v_cmp_ne_u32_e64 s[6:7], v3, v135
	v_lshl_add_u64 v[2:3], s[4:5], 0, v[86:87]
	s_mov_b64 s[4:5], 0x90000000
	v_writelane_b32 v254, s57, 1
	v_or_b32_e32 v6, 8, v86
	v_or_b32_e32 v7, 9, v86
	v_or_b32_e32 v8, 10, v86
	v_or_b32_e32 v9, 11, v86
	v_or_b32_e32 v10, 16, v86
	v_or_b32_e32 v11, 17, v86
	v_or_b32_e32 v12, 18, v86
	v_or_b32_e32 v13, 19, v86
	v_or_b32_e32 v14, 24, v86
	v_or_b32_e32 v15, 25, v86
	v_or_b32_e32 v16, 26, v86
	v_or_b32_e32 v17, 27, v86
	v_lshl_add_u64 v[88:89], v[2:3], 0, s[4:5]
	v_add_u32_e32 v2, s2, v192
	v_lshlrev_b32_e32 v3, 2, v85
	v_cmp_gt_u32_e64 s[36:37], 32, v1
	v_mul_u32_u24_e32 v1, 0x310, v85
	v_sub_u32_e32 v6, v6, v85
	v_sub_u32_e32 v7, v7, v85
	v_sub_u32_e32 v8, v8, v85
	v_sub_u32_e32 v9, v9, v85
	v_sub_u32_e32 v10, v10, v85
	v_sub_u32_e32 v11, v11, v85
	v_sub_u32_e32 v12, v12, v85
	v_sub_u32_e32 v13, v13, v85
	v_sub_u32_e32 v14, v14, v85
	v_sub_u32_e32 v15, v15, v85
	v_sub_u32_e32 v16, v16, v85
	v_sub_u32_e32 v17, v17, v85
	v_writelane_b32 v254, s6, 2
	v_sub_u32_e32 v87, v2, v3
	v_mul_u32_u24_e32 v2, 0x90, v85
	s_movk_i32 s2, 0x1200
	v_lshl_add_u64 v[82:83], s[94:95], 0, v[192:193]
	v_cndmask_b32_e64 v112, 0, 1.0, s[36:37]
	v_add_u32_e32 v84, 0, v192
	v_add_u32_e32 v114, 0xd800, v113
	v_cmp_gt_u32_e64 s[38:39], s33, v115
	v_cmp_gt_u32_e64 s[46:47], s33, v6
	v_cmp_gt_u32_e64 s[48:49], s33, v7
	v_cmp_gt_u32_e64 s[50:51], s33, v8
	v_cmp_gt_u32_e64 s[52:53], s33, v9
	v_cmp_gt_u32_e64 s[54:55], s33, v10
	v_cmp_gt_u32_e64 s[56:57], s33, v11
	v_cmp_gt_u32_e64 s[58:59], s33, v12
	v_cmp_gt_u32_e64 s[60:61], s33, v13
	v_cmp_gt_u32_e64 s[62:63], s33, v14
	v_cmp_gt_u32_e64 s[64:65], s33, v15
	v_cmp_gt_u32_e64 s[66:67], s33, v16
	v_cmp_gt_u32_e64 s[68:69], s33, v17
	v_lshl_add_u32 v136, v135, 9, v80
	v_writelane_b32 v254, s7, 3
	v_add3_u32 v137, v2, v192, s2
	v_lshl_or_b32 v138, v4, 3, v1
	s_mov_b32 s25, -1
	v_lshlrev_b32_e32 v192, 1, v0
	s_xor_b64 s[96:97], vcc, -1
	s_mov_b32 s24, s17
	s_branch .LBB0_307

; DI unsigned pk_fp8x4(float a, float b, float c, float d) { int p = 0; p = __builtin_amdgcn_cvt_pk_fp8_f32(a, b, p, false); p = __builtin_amdgcn_cvt_pk_fp8_f32(c, d, p, true); return (unsigned)p; }
; DI float other_half(float x, int h) { const u32x2 r = __builtin_amdgcn_permlane32_swap(__builtin_bit_cast(unsigned, x), __builtin_bit_cast(unsigned, x), false, false); return __builtin_bit_cast(float, h ? r.x : r.y); }
; #define REP(n) for (int rep_ = 0; rep_ < 1 + ((REPMASK >> (n)) & 1); ++rep_)
; #define IN(k) (lo <= (k) && (k) < hi && ((F = make_frame((LAS unsigned char*)lds_raw, wv)), true))
; #define SEAM(k) do { if ((k) + 1 < hi) xcd_barrier(bar, tid_now(wv) == 0); } while (0)
; DI void phase_attn(const Frame& F, int j) {
;     ...
;             const float inv = __builtin_amdgcn_rcpf(lrun + other_half(lrun, h)); unsigned char* orow = O + qrow * D + head * 64;
; #pragma unroll
;             for (int g4 = 0; g4 < 4; ++g4) { const int d0 = 8 * g4 + 4 * h;
;                 *(unsigned*)(orow + d0) = pk_fp8x4(O0[4 * g4] * inv, O0[4 * g4 + 1] * inv, O0[4 * g4 + 2] * inv, O0[4 * g4 + 3] * inv);
;                 *(unsigned*)(orow + 32 + d0) = pk_fp8x4(O1[4 * g4] * inv, O1[4 * g4 + 1] * inv, O1[4 * g4 + 2] * inv, O1[4 * g4 + 3] * inv); }
;         }
;     }
; }
; __global__ void __launch_bounds__(NTHR, 2) fwd_kernel(Args args) {
;     ...
;             REP(9) if (PM(9)) if (IN(pb + 1)) { phase_attn(F, j); SEAM(pb + 1); }
.LBB0_394:
	s_setprio 0
	v_readlane_b32 s58, v253, 45
	v_readlane_b32 s96, v253, 48
	v_readlane_b32 s50, v253, 50
	v_readlane_b32 s46, v253, 52
	v_readlane_b32 s56, v254, 0
	v_readlane_b32 s24, v254, 4
	v_readlane_b32 s94, v253, 44
	v_readlane_b32 s59, v253, 46
	v_readlane_b32 s60, v253, 47
	v_readlane_b32 s97, v253, 49
	v_readlane_b32 s51, v253, 51
	v_readlane_b32 s47, v253, 53
	v_readlane_b32 s57, v254, 1
	v_readlane_b32 s25, v254, 5
	s_mov_b64 s[30:31], 0

; #define LAS __attribute__((address_space(3)))
; DI float kf(float c) { asm volatile("" : "+v"(c)); return c; }
; DI void phase_rsub(const Frame& F, int j) {
;     const bf16_t* P = (const bf16_t*)(F.ws + WS_P); const bf16_t* LO = (const bf16_t*)(F.ws + WS_LO);
;     float* BS = (float*)(F.ws + WS_BS);
;     LAS unsigned char* wl = F.lds + F.wave * 16384;
;     const int k = F.lane; const float dk = kf(-0.60653066f);
;     for (int u = F.gw; u < NB * NSUB * RH; u += F.NGW) {
;         const int hd = u & 7, jj = (u >> 3) & (NSUB - 1), b = u >> 11, ch = hd * 64 + k, tt0 = 16 * jj;
;         float mp[3], mn[3];
; #pragma unroll
;         for (int q = 0; q < 3; ++q) { mp[q] = F.ap->in[9][(size_t)j * A_PROJ + q * 512 + ch]; mn[q] = F.ap->in[10][(size_t)j * A_PROJ + q * 512 + ch]; }
;         const float kkw = F.ap->in[15][j * 512 + ch], kaw = F.ap->in[16][j * 512 + ch], rkw = F.ap->in[17][j * 512 + ch];
;         const float w00 = F.ap->in[11][(j * 2 + 0) * 512 + ch], w01 = F.ap->in[11][(j * 2 + 1) * 512 + ch], a00 = F.ap->in[13][(j * 2 + 0) * 512 + ch], a01 = F.ap->in[13][(j * 2 + 1) * 512 + ch];
;     ...
;                     bsv = k == i ? bs : bsv;
.LBB0_551:
	s_ashr_i32 s8, s2, 6
	s_lshl_b32 s7, s7, 3
	s_add_i32 s42, s7, s8
	v_mov_b32_e32 v16, 0xbf1b4598
	s_cmpk_gt_i32 s42, 0x3fff
	s_cbranch_scc1 .LBB0_696
	s_cmp_lt_u32 s8, 4
	s_cbranch_scc1 .Lrsub_prio_done
	s_setprio 1
.Lrsub_prio_done:
	v_writelane_b32 v254, s56, 0
	v_and_b32_e32 v18, 63, v0
	s_lshl_b32 s6, s6, 3
	v_writelane_b32 v254, s57, 1
	s_lshl_b32 s8, s8, 14
	v_writelane_b32 v254, s6, 2
	s_add_i32 s44, s8, 0
	v_cmp_gt_u32_e64 s[8:9], 16, v18
	s_load_dwordx2 s[6:7], s[4:5], 0x128
	v_writelane_b32 v253, s17, 61
	v_writelane_b32 v254, s8, 4
	v_writelane_b32 v253, s62, 62
	s_waitcnt lgkmcnt(0)
	s_add_u32 s10, s6, 0xd3000000
	v_writelane_b32 v254, s9, 5
	v_cmp_eq_u32_e64 s[8:9], 15, v18
	v_writelane_b32 v253, s63, 63
	s_nop 0
	v_writelane_b32 v254, s8, 6
	v_readlane_b32 s12, v253, 59
	v_readlane_b32 s13, v253, 60
	v_writelane_b32 v254, s9, 7
	v_cmp_eq_u32_e64 s[8:9], 14, v18
	s_nop 1
	v_writelane_b32 v254, s8, 8
	s_nop 1
	v_writelane_b32 v254, s9, 9
	v_cmp_eq_u32_e64 s[8:9], 13, v18
	s_nop 1
	v_writelane_b32 v254, s8, 10
	s_nop 1
	v_writelane_b32 v254, s9, 11
	v_cmp_eq_u32_e64 s[8:9], 12, v18
	s_nop 1
	v_writelane_b32 v254, s8, 12
	s_nop 1
	v_writelane_b32 v254, s9, 13
	v_cmp_eq_u32_e64 s[8:9], 11, v18
	s_nop 1
	v_writelane_b32 v254, s8, 14
	s_nop 1
	v_writelane_b32 v254, s9, 15
	v_cmp_eq_u32_e64 s[8:9], 10, v18
	s_nop 1
	v_writelane_b32 v254, s8, 16
	s_nop 1
	v_writelane_b32 v254, s9, 17
	v_cmp_eq_u32_e64 s[8:9], 9, v18
	s_nop 1
	v_writelane_b32 v254, s8, 18
	s_nop 1
	v_writelane_b32 v254, s9, 19
	v_cmp_eq_u32_e64 s[8:9], 8, v18
	s_nop 1
	v_writelane_b32 v254, s8, 20
	s_nop 1
	v_writelane_b32 v254, s9, 21
	v_cmp_eq_u32_e64 s[8:9], 7, v18
	s_nop 1
	v_writelane_b32 v254, s8, 22
	s_nop 1
	v_writelane_b32 v254, s9, 23
	v_cmp_eq_u32_e64 s[8:9], 6, v18
	s_nop 1
	v_writelane_b32 v254, s8, 24
	s_nop 1
	v_writelane_b32 v254, s9, 25
	v_cmp_eq_u32_e64 s[8:9], 5, v18
	s_nop 1
	v_writelane_b32 v254, s8, 26
	s_nop 1
	v_writelane_b32 v254, s9, 27
	v_cmp_eq_u32_e64 s[8:9], 4, v18
	s_nop 1
	v_writelane_b32 v254, s8, 28
	s_nop 1
	v_writelane_b32 v254, s9, 29
	v_cmp_eq_u32_e64 s[8:9], 3, v18
	s_nop 1
	v_writelane_b32 v254, s8, 30
	s_nop 1
	v_writelane_b32 v254, s9, 31
	v_writelane_b32 v254, s10, 32
	s_addc_u32 s10, s7, 0
	v_writelane_b32 v254, s10, 33
	s_add_u32 s10, s6, 0xce000000
	v_writelane_b32 v254, s10, 34
	s_addc_u32 s10, s7, 0
	v_writelane_b32 v254, s10, 35
	s_add_u32 s10, s6, 0xba000000
	v_writelane_b32 v254, s10, 36
	s_addc_u32 s10, s7, 0
	v_writelane_b32 v254, s10, 37
	s_add_u32 s10, s6, 0xd2000000
	v_writelane_b32 v254, s10, 38
	s_addc_u32 s10, s7, 0
	v_writelane_b32 v254, s10, 39
	s_add_u32 s10, s6, 0xca000000
	s_load_dwordx4 s[36:39], s[4:5], 0x48
	s_load_dwordx2 s[8:9], s[4:5], 0x58
	s_load_dwordx2 s[22:23], s[4:5], 0x68
	s_load_dwordx4 s[48:51], s[4:5], 0x78
	s_nop 0
	s_load_dwordx2 s[4:5], s[4:5], 0x88
	s_addc_u32 s54, s7, 0
	s_bfe_u32 s2, s2, 0x30006
	v_lshl_or_b32 v2, s2, 6, v18
	v_add_u32_e32 v192, s12, v2
	v_lshlrev_b64 v[0:1], 2, v[192:193]
	v_or_b32_e32 v192, s28, v2
	s_waitcnt lgkmcnt(0)
	v_lshl_add_u64 v[20:21], s[36:37], 0, v[0:1]
	v_lshl_add_u64 v[22:23], s[38:39], 0, v[0:1]
	v_lshlrev_b64 v[0:1], 2, v[192:193]
	v_lshl_add_u64 v[32:33], s[4:5], 0, v[0:1]
	v_readlane_b32 s4, v253, 54
	v_lshl_add_u64 v[28:29], s[48:49], 0, v[0:1]
	v_lshl_add_u64 v[30:31], s[50:51], 0, v[0:1]
	v_lshl_or_b32 v192, s4, 10, v2
	v_readlane_b32 s5, v253, 55
	v_lshlrev_b64 v[0:1], 2, v[192:193]
	v_lshlrev_b32_e32 v192, 1, v2
	v_lshl_add_u64 v[34:35], s[8:9], 0, v[0:1]
	v_lshl_add_u64 v[36:37], s[22:23], 0, v[0:1]
	v_lshl_add_u64 v[0:1], s[6:7], 0, v[192:193]
	s_mov_b64 s[4:5], 0x38000000
	v_lshl_add_u64 v[38:39], v[0:1], 0, s[4:5]
	s_mov_b64 s[4:5], 0x44000000
	v_lshl_add_u64 v[40:41], v[0:1], 0, s[4:5]
	s_lshl_b32 s4, s2, 2
	s_add_u32 s4, s6, s4
	s_addc_u32 s5, s7, 0
	s_add_u32 s4, s4, 0x72000000
	v_writelane_b32 v254, s10, 40
	s_addc_u32 s5, s5, 0
	v_writelane_b32 v254, s4, 41
	s_lshl_b32 s2, s2, 9
	v_lshl_add_u64 v[24:25], v[20:21], 0, s[0:1]
	v_writelane_b32 v254, s5, 42
	v_writelane_b32 v254, s2, 43
	s_add_i32 s2, s44, 0x1248
	v_writelane_b32 v254, s2, 44
	s_add_i32 s2, s44, 0x128c
	v_writelane_b32 v254, s2, 45
	s_add_i32 s2, s44, 0x1314
	v_writelane_b32 v254, s2, 46
	s_add_i32 s2, s44, 0x1358
	v_writelane_b32 v254, s2, 47
	s_add_i32 s2, s44, 0x139c
	v_writelane_b32 v254, s2, 48
	s_add_i32 s2, s44, 0x1424
	v_writelane_b32 v254, s2, 49
	s_add_i32 s2, s44, 0x1468
	v_writelane_b32 v254, s2, 50
	s_add_i32 s2, s44, 0x14ac
	v_writelane_b32 v254, s2, 51
	s_add_i32 s2, s44, 0x1534
	v_writelane_b32 v254, s2, 52
	s_add_i32 s2, s44, 0x14b4
	v_writelane_b32 v254, s2, 53
	s_add_i32 s2, s44, 0x142c
	v_writelane_b32 v254, s2, 54
	s_add_i32 s2, s44, 0x1434
	v_writelane_b32 v254, s2, 55
	s_add_i32 s2, s44, 0x13a4
	v_writelane_b32 v254, s2, 56
	s_add_i32 s2, s44, 0x13ac
	v_writelane_b32 v254, s2, 57
	s_add_i32 s2, s44, 0x13b4
	v_writelane_b32 v254, s2, 58
	s_add_i32 s2, s44, 0x1368
	v_writelane_b32 v254, s2, 59
	s_add_i32 s2, s44, 0x131c
	v_writelane_b32 v254, s2, 60
	s_add_i32 s2, s44, 0x1324
	v_writelane_b32 v254, s2, 61
	s_add_i32 s2, s44, 0x132c
	v_writelane_b32 v254, s2, 62
	s_add_i32 s2, s44, 0x1334
	v_writelane_b32 v254, s2, 63
	s_add_i32 s2, s44, 0x1294
	v_writelane_b32 v255, s2, 0
	s_add_i32 s2, s44, 0x129c
	v_writelane_b32 v255, s2, 1
	s_add_i32 s2, s44, 0x12a4
	v_writelane_b32 v255, s2, 2
	s_add_i32 s2, s44, 0x12ac
	v_writelane_b32 v255, s2, 3
	s_add_i32 s2, s44, 0x12b4
	v_writelane_b32 v255, s2, 4
	s_add_i32 s2, s44, 0x1258
	v_writelane_b32 v255, s2, 5
	s_add_i32 s2, s44, 0x1268
	v_writelane_b32 v255, s2, 6
	s_add_i32 s2, s44, 0x1204
	v_writelane_b32 v255, s2, 7
	s_add_i32 s2, s44, 0x120c
	v_writelane_b32 v255, s2, 8
	s_add_i32 s2, s44, 0x1214
	v_writelane_b32 v255, s2, 9
	s_add_i32 s2, s44, 0x121c
	v_writelane_b32 v255, s2, 10
	s_add_i32 s2, s44, 0x1224
	v_writelane_b32 v255, s2, 11
	s_add_i32 s2, s44, 0x122c
	v_writelane_b32 v255, s2, 12
	s_add_i32 s2, s44, 0x1234
	v_writelane_b32 v255, s2, 13
	v_cmp_eq_u32_e64 s[4:5], 2, v18
	v_lshl_add_u64 v[26:27], v[22:23], 0, s[0:1]
	s_nop 0
	v_writelane_b32 v255, s4, 14
	s_nop 1
	v_writelane_b32 v255, s5, 15
	v_cmp_eq_u32_e64 s[4:5], 1, v18
	s_nop 1
	v_writelane_b32 v255, s4, 16
	s_nop 1
	v_writelane_b32 v255, s5, 17
	v_cmp_eq_u32_e64 s[4:5], 0, v18
	s_nop 1
	v_writelane_b32 v255, s4, 18
	s_nop 1
	v_writelane_b32 v255, s5, 19
	v_writelane_b32 v255, s24, 20
	s_nop 1
	v_writelane_b32 v255, s25, 21
	s_branch .LBB0_554

; DI unsigned xb_add(unsigned* p, unsigned v) { return __hip_atomic_fetch_add(p, v, __ATOMIC_RELAXED, __HIP_MEMORY_SCOPE_AGENT); }
; #define REP(n) for (int rep_ = 0; rep_ < 1 + ((REPMASK >> (n)) & 1); ++rep_)
; #define IN(k) (lo <= (k) && (k) < hi && ((F = make_frame((LAS unsigned char*)lds_raw, wv)), true))
; #define SEAM(k) do { if ((k) + 1 < hi) xcd_barrier(bar, tid_now(wv) == 0); } while (0)
; DI void xcd_barrier(const XcdBarrier& b, const bool leader) {
;     asm volatile("s_waitcnt vmcnt(0)" ::: "memory");
;     __syncthreads();
;     if (leader) {
;         unsigned* bar = b.bar;
;         __builtin_amdgcn_s_waitcnt(0);
;         unsigned nloc = b.st[0], nx = b.st[1];
;         if (nloc == 0u) { xcd_barrier_complete(bar, b.x, nloc, nx); b.st[0] = nloc; b.st[1] = nx; }
;         const unsigned old = xb_add(&bar[XB_XSUB(b.x)], 1u);
; __global__ void __launch_bounds__(NTHR, 2) fwd_kernel(Args args) {
;     ...
;             REP(6) if (PM(6)) if (IN(pb + 4)) { phase_rsub(F, j); SEAM(pb + 4); }
.LBB0_696:
	s_setprio 0
	s_andn2_b64 vcc, exec, s[24:25]
	s_cbranch_vccnz .LBB0_746
	v_mbcnt_lo_u32_b32 v0, -1, 0
	v_mbcnt_hi_u32_b32 v0, -1, v0
	s_waitcnt vmcnt(0)
	v_readlane_b32 s2, v252, 4
	s_waitcnt vmcnt(0)
	s_barrier
	v_cmp_eq_u32_e32 vcc, s2, v0
	s_and_saveexec_b64 s[36:37], vcc
	s_cbranch_execz .LBB0_745
	v_readlane_b32 s2, v252, 3
	s_waitcnt vmcnt(0) expcnt(0) lgkmcnt(0)
	s_nop 0
	v_mov_b32_e32 v0, s2
	ds_read_b32 v2, v0
	ds_read_b32 v0, v0 offset:4
	s_waitcnt lgkmcnt(1)
	v_cmp_ne_u32_e32 vcc, 0, v2
	s_cbranch_vccnz .LBB0_713
	v_readlane_b32 s6, v252, 1
	v_readlane_b32 s7, v252, 2
	s_load_dwordx2 s[4:5], s[6:7], 0x4
	s_mov_b32 s10, 1
	s_waitcnt lgkmcnt(0)
	s_mul_i32 s2, s4, s60
	s_mul_i32 s2, s2, s5
	s_branch .LBB0_701
